# plainst
# speedup vs baseline: 1.0110x; 1.0110x over previous
.Lenc_skip2:
	s_or_b64 exec, exec, s[10:11]
	v_lshrrev_b32_e32 v45, 5, v0
	v_and_b32_e32 v54, 4, v45
	v_mul_u32_u24_e32 v58, 0xa0, v54
	s_waitcnt lgkmcnt(0)
	s_barrier
	ds_read_b128 v[46:49], v58
	ds_read_b128 v[50:53], v58 offset:16
	v_mov_b32_e32 v3, 0
	v_lshl_add_u64 v[4:5], s[6:7], 0, v[2:3]
	s_mov_b64 s[4:5], 0x16000
	s_waitcnt vmcnt(0) lgkmcnt(1)
	v_fma_f32 v55, v46, v41, v1
	v_fmac_f32_e32 v55, v47, v39
	v_fmac_f32_e32 v55, v48, v37
	v_fmac_f32_e32 v55, v49, v36
	ds_read_b128 v[46:49], v58 offset:32
	s_waitcnt lgkmcnt(1)
	v_fmac_f32_e32 v55, v50, v35
	v_fmac_f32_e32 v55, v51, v34
	v_fmac_f32_e32 v55, v52, v33
	v_fmac_f32_e32 v55, v53, v32
	ds_read_b128 v[50:53], v58 offset:48
	s_waitcnt lgkmcnt(1)
	v_fmac_f32_e32 v55, v46, v42
	v_fmac_f32_e32 v55, v47, v44
	v_fmac_f32_e32 v55, v48, v43
	v_fmac_f32_e32 v55, v49, v40
	ds_read_b128 v[46:49], v58 offset:64
	s_waitcnt lgkmcnt(1)
	v_fmac_f32_e32 v55, v50, v38
	v_fmac_f32_e32 v55, v51, v26
	v_fmac_f32_e32 v55, v52, v27
	v_fmac_f32_e32 v55, v53, v28
	ds_read_b128 v[50:53], v58 offset:80
	s_waitcnt lgkmcnt(1)
	v_fmac_f32_e32 v55, v46, v24
	v_fmac_f32_e32 v55, v47, v29
	v_fmac_f32_e32 v55, v48, v30
	v_fmac_f32_e32 v55, v49, v31
	ds_read_b128 v[46:49], v58 offset:96
	s_waitcnt lgkmcnt(1)
	v_fmac_f32_e32 v55, v50, v25
	v_fmac_f32_e32 v55, v51, v18
	v_fmac_f32_e32 v55, v52, v19
	v_fmac_f32_e32 v55, v53, v20
	ds_read_b128 v[50:53], v58 offset:112
	s_waitcnt lgkmcnt(1)
	v_fmac_f32_e32 v55, v46, v16
	v_fmac_f32_e32 v55, v47, v21
	v_fmac_f32_e32 v55, v48, v22
	v_fmac_f32_e32 v55, v49, v23
	ds_read_b128 v[46:49], v58 offset:128
	s_waitcnt lgkmcnt(1)
	v_fmac_f32_e32 v55, v50, v17
	v_fmac_f32_e32 v55, v51, v10
	v_fmac_f32_e32 v55, v52, v11
	v_fmac_f32_e32 v55, v53, v12
	ds_read_b96 v[50:52], v58 offset:144
	s_waitcnt lgkmcnt(1)
	v_fmac_f32_e32 v55, v46, v7
	v_fmac_f32_e32 v55, v47, v13
	v_fmac_f32_e32 v55, v48, v14
	v_fmac_f32_e32 v55, v49, v15
	ds_read_b128 v[46:49], v58 offset:160
	s_waitcnt lgkmcnt(1)
	v_fmac_f32_e32 v55, v50, v9
	v_add_u32_e32 v2, s3, v54
	v_lshl_add_u64 v[4:5], v[4:5], 0, s[4:5]
	v_fmac_f32_e32 v55, v51, v8
	v_lshlrev_b64 v[50:51], 9, v[2:3]
	v_fmac_f32_e32 v55, v52, v6
	v_lshl_add_u64 v[50:51], v[4:5], 0, v[50:51]
	v_mul_f32_e32 v55, 0xf800000, v55
	global_store_dword v[50:51], v55, off
	ds_read_b128 v[50:53], v58 offset:176
	s_waitcnt lgkmcnt(1)
	v_fma_f32 v54, v46, v41, v1
	v_fmac_f32_e32 v54, v47, v39
	v_fmac_f32_e32 v54, v48, v37
	v_fmac_f32_e32 v54, v49, v36
	ds_read_b128 v[46:49], v58 offset:192
	s_waitcnt lgkmcnt(1)
	v_fmac_f32_e32 v54, v50, v35
	v_fmac_f32_e32 v54, v51, v34
	v_fmac_f32_e32 v54, v52, v33
	v_fmac_f32_e32 v54, v53, v32
	ds_read_b128 v[50:53], v58 offset:208
	s_waitcnt lgkmcnt(1)
	v_fmac_f32_e32 v54, v46, v42
	v_fmac_f32_e32 v54, v47, v44
	v_fmac_f32_e32 v54, v48, v43
	v_fmac_f32_e32 v54, v49, v40
	ds_read_b128 v[46:49], v58 offset:224
	s_waitcnt lgkmcnt(1)
	v_fmac_f32_e32 v54, v50, v38
	v_fmac_f32_e32 v54, v51, v26
	v_fmac_f32_e32 v54, v52, v27
	v_fmac_f32_e32 v54, v53, v28
	ds_read_b128 v[50:53], v58 offset:240
	s_waitcnt lgkmcnt(1)
	v_fmac_f32_e32 v54, v46, v24
	v_fmac_f32_e32 v54, v47, v29
	v_fmac_f32_e32 v54, v48, v30
	v_fmac_f32_e32 v54, v49, v31
	ds_read_b128 v[46:49], v58 offset:256
	s_waitcnt lgkmcnt(1)
	v_fmac_f32_e32 v54, v50, v25
	v_fmac_f32_e32 v54, v51, v18
	v_fmac_f32_e32 v54, v52, v19
	v_fmac_f32_e32 v54, v53, v20
	ds_read_b128 v[50:53], v58 offset:272
	s_waitcnt lgkmcnt(1)
	v_fmac_f32_e32 v54, v46, v16
	v_fmac_f32_e32 v54, v47, v21
	v_fmac_f32_e32 v54, v48, v22
	v_fmac_f32_e32 v54, v49, v23
	ds_read_b128 v[46:49], v58 offset:288
	s_waitcnt lgkmcnt(1)
	v_fmac_f32_e32 v54, v50, v17
	v_fmac_f32_e32 v54, v51, v10
	v_fmac_f32_e32 v54, v52, v11
	v_fmac_f32_e32 v54, v53, v12
	ds_read_b96 v[50:52], v58 offset:304
	s_waitcnt lgkmcnt(1)
	v_fmac_f32_e32 v54, v46, v7
	v_fmac_f32_e32 v54, v47, v13
	v_fmac_f32_e32 v54, v48, v14
	v_fmac_f32_e32 v54, v49, v15
	s_waitcnt lgkmcnt(0)
	v_fmac_f32_e32 v54, v50, v9
	ds_read_b128 v[46:49], v58 offset:320
	v_fmac_f32_e32 v54, v51, v8
	v_add_u32_e32 v50, 1, v2
	v_mov_b32_e32 v51, v3
	v_lshlrev_b64 v[50:51], 9, v[50:51]
	v_fmac_f32_e32 v54, v52, v6
	v_lshl_add_u64 v[50:51], v[4:5], 0, v[50:51]
	v_mul_f32_e32 v54, 0xf800000, v54
	global_store_dword v[50:51], v54, off
	ds_read_b128 v[50:53], v58 offset:336
	s_waitcnt lgkmcnt(1)
	v_fma_f32 v59, v46, v41, v1
	v_fmac_f32_e32 v59, v47, v39
	v_fmac_f32_e32 v59, v48, v37
	v_fmac_f32_e32 v59, v49, v36
	ds_read_b128 v[46:49], v58 offset:352
	ds_read_b128 v[54:57], v58 offset:368
	s_waitcnt lgkmcnt(2)
	v_fmac_f32_e32 v59, v50, v35
	v_fmac_f32_e32 v59, v51, v34
	v_fmac_f32_e32 v59, v52, v33
	v_fmac_f32_e32 v59, v53, v32
	s_waitcnt lgkmcnt(1)
	v_fmac_f32_e32 v59, v46, v42
	v_fmac_f32_e32 v59, v47, v44
	v_fmac_f32_e32 v59, v48, v43
	v_fmac_f32_e32 v59, v49, v40
	ds_read_b128 v[46:49], v58 offset:384
	ds_read_b128 v[50:53], v58 offset:400
	s_waitcnt lgkmcnt(2)
	v_fmac_f32_e32 v59, v54, v38
	v_fmac_f32_e32 v59, v55, v26
	v_fmac_f32_e32 v59, v56, v27
	v_fmac_f32_e32 v59, v57, v28
	s_waitcnt lgkmcnt(1)
	v_fmac_f32_e32 v59, v46, v24
	v_fmac_f32_e32 v59, v47, v29
	v_fmac_f32_e32 v59, v48, v30
	v_fmac_f32_e32 v59, v49, v31
	ds_read_b128 v[46:49], v58 offset:416
	s_waitcnt lgkmcnt(1)
	v_fmac_f32_e32 v59, v50, v25
	v_fmac_f32_e32 v59, v51, v18
	v_fmac_f32_e32 v59, v52, v19
	v_fmac_f32_e32 v59, v53, v20
	ds_read_b128 v[50:53], v58 offset:432
	s_waitcnt lgkmcnt(1)
	v_fmac_f32_e32 v59, v46, v16
	v_fmac_f32_e32 v59, v47, v21
	v_fmac_f32_e32 v59, v48, v22
	v_fmac_f32_e32 v59, v49, v23
	ds_read_b128 v[46:49], v58 offset:448
	s_waitcnt lgkmcnt(1)
	v_fmac_f32_e32 v59, v50, v17
	v_fmac_f32_e32 v59, v51, v10
	v_fmac_f32_e32 v59, v52, v11
	v_fmac_f32_e32 v59, v53, v12
	ds_read_b96 v[50:52], v58 offset:464
	s_waitcnt lgkmcnt(1)
	v_fmac_f32_e32 v59, v46, v7
	v_fmac_f32_e32 v59, v47, v13
	v_or_b32_e32 v45, 3, v45
	v_fmac_f32_e32 v59, v48, v14
	v_mul_u32_u24_e32 v62, 0xa0, v45
	v_fmac_f32_e32 v59, v49, v15
	ds_read_b128 v[46:49], v62
	s_waitcnt lgkmcnt(1)
	v_fmac_f32_e32 v59, v50, v9
	v_add_u32_e32 v2, 2, v2
	v_fmac_f32_e32 v59, v51, v8
	v_lshlrev_b64 v[50:51], 9, v[2:3]
	v_fmac_f32_e32 v59, v52, v6
	v_lshl_add_u64 v[50:51], v[4:5], 0, v[50:51]
	v_mul_f32_e32 v59, 0xf800000, v59
	global_store_dword v[50:51], v59, off
	ds_read_b128 v[50:53], v62 offset:16
	s_waitcnt lgkmcnt(1)
	v_fmac_f32_e32 v1, v46, v41
	v_fmac_f32_e32 v1, v47, v39
	v_fmac_f32_e32 v1, v48, v37
	v_fmac_f32_e32 v1, v49, v36
	ds_read_b128 v[54:57], v62 offset:32
	ds_read_b128 v[58:61], v62 offset:48
	s_waitcnt lgkmcnt(2)
	v_fmac_f32_e32 v1, v50, v35
	v_fmac_f32_e32 v1, v51, v34
	v_fmac_f32_e32 v1, v52, v33
	v_fmac_f32_e32 v1, v53, v32
	s_waitcnt lgkmcnt(1)
	v_fmac_f32_e32 v1, v54, v42
	v_fmac_f32_e32 v1, v55, v44
	v_fmac_f32_e32 v1, v56, v43
	v_fmac_f32_e32 v1, v57, v40
	ds_read_b128 v[32:35], v62 offset:64
	s_waitcnt lgkmcnt(1)
	v_fmac_f32_e32 v1, v58, v38
	v_fmac_f32_e32 v1, v59, v26
	v_fmac_f32_e32 v1, v60, v27
	v_fmac_f32_e32 v1, v61, v28
	ds_read_b128 v[36:39], v62 offset:80
	s_waitcnt lgkmcnt(1)
	v_fmac_f32_e32 v1, v32, v24
	v_fmac_f32_e32 v1, v33, v29
	v_fmac_f32_e32 v1, v34, v30
	v_fmac_f32_e32 v1, v35, v31
	s_waitcnt lgkmcnt(0)
	v_fmac_f32_e32 v1, v36, v25
	ds_read_b128 v[24:27], v62 offset:96
	ds_read_b128 v[28:31], v62 offset:112
	v_fmac_f32_e32 v1, v37, v18
	v_fmac_f32_e32 v1, v38, v19
	v_fmac_f32_e32 v1, v39, v20
	s_waitcnt lgkmcnt(1)
	v_fmac_f32_e32 v1, v24, v16
	v_fmac_f32_e32 v1, v25, v21
	v_fmac_f32_e32 v1, v26, v22
	v_fmac_f32_e32 v1, v27, v23
	s_waitcnt lgkmcnt(0)
	v_fmac_f32_e32 v1, v28, v17
	ds_read_b128 v[16:19], v62 offset:128
	v_fmac_f32_e32 v1, v29, v10
	v_fmac_f32_e32 v1, v30, v11
	v_fmac_f32_e32 v1, v31, v12
	ds_read_b96 v[10:12], v62 offset:144
	s_waitcnt lgkmcnt(1)
	v_fmac_f32_e32 v1, v16, v7
	v_fmac_f32_e32 v1, v17, v13
	v_fmac_f32_e32 v1, v18, v14
	v_fmac_f32_e32 v1, v19, v15
	s_waitcnt lgkmcnt(0)
	v_fmac_f32_e32 v1, v10, v9
	v_add_u32_e32 v2, s3, v45
	v_fmac_f32_e32 v1, v11, v8
	v_lshlrev_b64 v[2:3], 9, v[2:3]
	v_fmac_f32_e32 v1, v12, v6
	v_lshl_add_u64 v[2:3], v[4:5], 0, v[2:3]
	v_mul_f32_e32 v1, 0xf800000, v1
	global_store_dword v[2:3], v1, off
	s_mov_b64 s[4:5], 0

.LBB0_30:
	s_andn2_saveexec_b64 s[4:5], s[10:11]
	v_mov_b32_e32 v13, 0.5
	v_fmamk_f32 v13, v14, 0xbeaaaaab, v13
	v_fma_f32 v13, -v14, v13, 1.0
	v_mul_f32_e32 v13, v14, v13
	s_or_b64 exec, exec, s[4:5]
	v_max_f32_e32 v10, v10, v10
	v_max_f32_e32 v10, 0, v10
	v_add_f32_e32 v10, v10, v12
	s_waitcnt vmcnt(3)
	v_mul_f32_e32 v9, v9, v10
	v_mul_f32_e32 v10, 0x41c80000, v9
	s_mov_b32 s3, 0x3c23d70a
	v_cmp_ngt_f32_e32 vcc, s3, v10
	s_and_saveexec_b64 s[4:5], vcc
	s_xor_b64 s[4:5], exec, s[4:5]
	v_mul_f32_e32 v9, 0xbfb8aa3b, v10
	v_exp_f32_e32 v9, v9
	s_nop 0
	v_sub_f32_e32 v9, 1.0, v9
	s_andn2_saveexec_b64 s[4:5], s[4:5]
	v_mov_b32_e32 v9, 0.5
	v_fmamk_f32 v9, v10, 0xbe2aaaab, v9
	v_fma_f32 v9, -v10, v9, 1.0
	v_mul_f32_e32 v9, v10, v9
	s_or_b64 exec, exec, s[4:5]
	v_max_f32_e32 v10, v11, v11
	v_max_f32_e32 v10, 0, v10
	v_add_f32_e32 v10, v10, v13
	s_waitcnt vmcnt(2)
	v_mul_f32_e32 v8, v8, v10
	v_mul_f32_e32 v10, 0x41c80000, v8
	v_cmp_ngt_f32_e32 vcc, s3, v10
	s_and_saveexec_b64 s[4:5], vcc
	s_xor_b64 s[4:5], exec, s[4:5]
	v_mul_f32_e32 v8, 0xbfb8aa3b, v10
	v_exp_f32_e32 v8, v8
	s_nop 0
	v_sub_f32_e32 v8, 1.0, v8
	s_andn2_saveexec_b64 s[4:5], s[4:5]
	v_mov_b32_e32 v8, 0.5
	v_fmamk_f32 v8, v10, 0xbe2aaaab, v8
	v_fma_f32 v8, -v10, v8, 1.0
	v_mul_f32_e32 v8, v10, v8
	s_or_b64 exec, exec, s[4:5]
	v_cmp_eq_u32_e32 vcc, 63, v7
	v_mov_b32_e32 v12, 1.0
	v_mov_b32_e32 v11, 1.0
	v_cndmask_b32_e64 v7, v8, 1.0, vcc
	v_sub_f32_e32 v8, 1.0, v9
	v_add_f32_e32 v8, 0x2edbe6ff, v8
	v_sub_f32_e32 v10, 1.0, v7
	v_add_f32_e32 v10, 0x2edbe6ff, v10
	v_mov_b32_dpp v12, v8 row_shr:1 row_mask:0xf bank_mask:0xf
	v_mul_f32_e32 v8, v8, v12
	v_mov_b32_e32 v12, 1.0
	v_lshl_add_u64 v[4:5], v[4:5], 2, s[6:7]
	s_mov_b64 s[4:5], 0x216000
	v_mov_b32_dpp v12, v8 row_shr:2 row_mask:0xf bank_mask:0xf
	v_mul_f32_e32 v8, v8, v12
	v_mov_b32_e32 v12, 1.0
	s_nop 1
	v_mov_b32_dpp v12, v8 row_shr:4 row_mask:0xf bank_mask:0xf
	v_mul_f32_e32 v8, v8, v12
	v_mov_b32_e32 v12, 1.0
	s_nop 1
	v_mov_b32_dpp v12, v8 row_shr:8 row_mask:0xf bank_mask:0xf
	v_mul_f32_e32 v8, v8, v12
	v_mov_b32_e32 v12, 1.0
	s_nop 1
	v_mov_b32_dpp v12, v8 row_bcast:15 row_mask:0xa bank_mask:0xf
	v_mul_f32_e32 v8, v8, v12
	v_mov_b32_e32 v12, 1.0
	s_nop 1
	v_mov_b32_dpp v12, v8 row_bcast:31 row_mask:0xc bank_mask:0xf
	v_mul_f32_e32 v8, v8, v12
	v_mov_b32_e32 v12, 1.0
	v_readlane_b32 s3, v8, 63
	s_nop 0
	v_mov_b32_dpp v12, v10 row_shr:1 row_mask:0xf bank_mask:0xf
	v_mul_f32_e32 v10, v10, v12
	v_mov_b32_e32 v12, 1.0
	s_nop 1
	v_mov_b32_dpp v12, v10 row_shr:2 row_mask:0xf bank_mask:0xf
	v_mul_f32_e32 v10, v10, v12
	v_mov_b32_e32 v12, 1.0
	s_nop 1
	v_mov_b32_dpp v12, v10 row_shr:4 row_mask:0xf bank_mask:0xf
	v_mul_f32_e32 v10, v10, v12
	v_mov_b32_e32 v12, 1.0
	s_nop 1
	v_mov_b32_dpp v12, v10 row_shr:8 row_mask:0xf bank_mask:0xf
	v_mul_f32_e32 v10, v10, v12
	v_mov_b32_e32 v12, 1.0
	s_nop 1
	v_mov_b32_dpp v12, v10 row_bcast:15 row_mask:0xa bank_mask:0xf
	v_mul_f32_e32 v10, v10, v12
	v_mov_b32_e32 v12, 1.0
	s_nop 1
	v_mov_b32_dpp v12, v10 row_bcast:31 row_mask:0xc bank_mask:0xf
	v_mul_f32_e32 v10, v10, v12
	v_mov_b32_e32 v12, 1.0
	s_nop 0
	v_mov_b32_dpp v11, v10 wave_shr:1 row_mask:0xf bank_mask:0xf
	v_mul_f32_e32 v10, s3, v11
	s_mov_b32 s3, 0x216000
	v_mov_b32_dpp v12, v8 wave_shr:1 row_mask:0xf bank_mask:0xf
	v_mul_f32_e32 v13, v7, v10
	v_lshl_add_u64 v[10:11], v[4:5], 0, s[4:5]
	v_add_co_u32_e64 v4, s[4:5], s3, v4
	v_mul_f32_e32 v8, v9, v12
	s_nop 0
	v_addc_co_u32_e64 v5, s[4:5], 0, v5, s[4:5]
	s_waitcnt vmcnt(0)
	v_mul_f32_e32 v6, v6, v13
	global_store_dword v[4:5], v8, off
	global_store_dword v[10:11], v13, off offset:256
	v_fma_f32 v5, v9, v12, v13
	v_fmac_f32_e32 v6, v1, v8
	v_mov_b32_e32 v7, 0
	v_add_f32_dpp v5, v5, v5 row_shr:1 row_mask:0xf bank_mask:0xf bound_ctrl:1
	v_add_f32_dpp v1, v6, v6 row_shr:1 row_mask:0xf bank_mask:0xf bound_ctrl:1
	v_mov_b32_e32 v6, 0
	v_add_f32_dpp v5, v5, v5 row_shr:2 row_mask:0xf bank_mask:0xf bound_ctrl:1
	v_add_f32_dpp v1, v1, v1 row_shr:2 row_mask:0xf bank_mask:0xf bound_ctrl:1
	v_mov_b32_e32 v4, 0
	v_add_f32_dpp v5, v5, v5 row_shr:4 row_mask:0xf bank_mask:0xf bound_ctrl:1
	v_add_f32_dpp v1, v1, v1 row_shr:4 row_mask:0xf bank_mask:0xf bound_ctrl:1
	s_nop 0
	v_add_f32_dpp v5, v5, v5 row_shr:8 row_mask:0xf bank_mask:0xf bound_ctrl:1
	v_add_f32_dpp v1, v1, v1 row_shr:8 row_mask:0xf bank_mask:0xf bound_ctrl:1
	s_nop 0
	v_mov_b32_dpp v7, v5 row_bcast:15 row_mask:0xa bank_mask:0xf
	v_mov_b32_dpp v6, v1 row_bcast:15 row_mask:0xa bank_mask:0xf
	v_add_f32_e32 v5, v5, v7
	v_mov_b32_e32 v7, 0
	v_add_f32_e32 v1, v1, v6
	s_nop 0
	v_mov_b32_dpp v7, v5 row_bcast:31 row_mask:0xc bank_mask:0xf
	v_mov_b32_dpp v4, v1 row_bcast:31 row_mask:0xc bank_mask:0xf
	s_and_saveexec_b64 s[4:5], vcc
	s_cbranch_execz .LBB0_42
	s_load_dwordx2 s[10:11], s[0:1], 0x48
	v_add_f32_e32 v1, v1, v4
	v_add_f32_e32 v6, v5, v7
	s_waitcnt lgkmcnt(0)
	v_lshl_add_u64 v[2:3], v[2:3], 2, s[10:11]
	v_add_co_u32_e32 v4, vcc, 0xc000, v2
	s_nop 1
	v_addc_co_u32_e32 v5, vcc, 0, v3, vcc
	v_add_co_u32_e32 v2, vcc, 0x10000, v2
	global_store_dword v[4:5], v1, off
	s_nop 0
	v_addc_co_u32_e32 v3, vcc, 0, v3, vcc
	global_store_dword v[2:3], v6, off
